# grid barrier: acquire invalidate (buffer_inv sc1) issued before the flag spin instead of after it, L1 stays empty while parked
# speedup vs baseline: 1.0157x; 1.0104x over previous
; __device__ __forceinline__ unsigned xb_ld(unsigned* p)              { return __hip_atomic_load(p, __ATOMIC_RELAXED, __HIP_MEMORY_SCOPE_AGENT); }
; __device__ __forceinline__ unsigned xb_add(unsigned* p, unsigned v) { return __hip_atomic_fetch_add(p, v, __ATOMIC_RELAXED, __HIP_MEMORY_SCOPE_AGENT); }
; #define XB_SPIN(cond, bar) do { unsigned _sp = 0; while (cond) { __builtin_amdgcn_s_sleep(1); \
;     if ((++_sp & 255u) == 0u) { if (xb_ld(&(bar)[XB_TMO])) break; if (_sp > XB_SPIN_CAP) { atomicAdd(&(bar)[XB_TMO], 1u); break; } } } } while (0)
; __device__ __forceinline__ void xcd_barrier(const XcdBarrier& b) {
;     ...
;         const unsigned old = xb_add(&bar[XB_XSUB(b.x)], 1u);
;         const unsigned gen = old / nloc;
;         if (old + 1u == (gen + 1u) * nloc) {
;             __builtin_amdgcn_fence(__ATOMIC_RELEASE, "agent");
;             asm volatile("s_waitcnt vmcnt(0)" ::: "memory");
;             const unsigned og = xb_add(&bar[XB_TOP], 1u);
;             const unsigned tg = og / nx;
;             if (og + 1u == (tg + 1u) * nx) xb_add(&bar[XB_TOPGEN], 1u);
;             else XB_SPIN(xb_ld(&bar[XB_TOPGEN]) == tg, bar);
;             __builtin_amdgcn_fence(__ATOMIC_ACQUIRE, "agent");
;             xb_add(&bar[XB_XGEN(b.x)], 1u);
;             asm volatile("s_waitcnt vmcnt(0)" ::: "memory");
;         } else {
;             XB_SPIN(xb_ld(&bar[XB_XGEN(b.x)]) == gen, bar);
;             __builtin_amdgcn_fence(__ATOMIC_ACQUIRE, "agent");
.LBB0_244:
	s_or_b64 exec, exec, s[12:13]
	v_cvt_f32_u32_e32 v4, v2
	s_waitcnt vmcnt(0)
	v_readfirstlane_b32 s10, v3
	v_sub_u32_e32 v3, 0, v2
	v_rcp_iflag_f32_e32 v4, v4
	v_add_u32_e32 v5, s10, v1
	v_mul_f32_e32 v4, 0x4f7ffffe, v4
	v_cvt_u32_f32_e32 v4, v4
	v_mul_lo_u32 v1, v3, v4
	v_mul_hi_u32 v1, v4, v1
	v_add_u32_e32 v1, v4, v1
	v_mul_hi_u32 v1, v5, v1
	v_mul_lo_u32 v3, v1, v2
	v_sub_u32_e32 v3, v5, v3
	v_add_u32_e32 v4, 1, v1
	v_cmp_ge_u32_e32 vcc, v3, v2
	s_nop 1
	v_cndmask_b32_e32 v1, v1, v4, vcc
	v_sub_u32_e32 v4, v3, v2
	v_cndmask_b32_e32 v3, v3, v4, vcc
	v_add_u32_e32 v4, 1, v1
	v_cmp_ge_u32_e32 vcc, v3, v2
	v_add_u32_e32 v3, 1, v5
	s_nop 0
	v_cndmask_b32_e32 v1, v1, v4, vcc
	v_mul_lo_u32 v4, v2, v1
	v_add_u32_e32 v2, v4, v2
	v_cmp_ne_u32_e32 vcc, v3, v2
	s_and_saveexec_b64 s[10:11], vcc
	s_xor_b64 s[10:11], exec, s[10:11]
	s_cbranch_execz .LBB0_258
	buffer_inv sc1
	s_waitcnt lgkmcnt(0)
	v_mov_b32_e32 v0, 0x2000
	global_load_dword v0, v0, s[8:9] offset:1024 sc1
	s_add_u32 s16, s8, 0x2400
	s_addc_u32 s17, s9, 0
	s_waitcnt vmcnt(0)
	v_cmp_eq_u32_e32 vcc, v0, v1
	s_and_saveexec_b64 s[12:13], vcc
	s_cbranch_execz .LBB0_257
	s_add_u32 s14, s0, 0x4200
	s_addc_u32 s15, s1, 0
	s_mov_b32 s28, 1
	s_mov_b64 s[18:19], 0
	v_mov_b32_e32 v0, 0
	s_branch .LBB0_248

; __device__ __forceinline__ unsigned xb_ld(unsigned* p)              { return __hip_atomic_load(p, __ATOMIC_RELAXED, __HIP_MEMORY_SCOPE_AGENT); }
; #define XB_SPIN(cond, bar) do { unsigned _sp = 0; while (cond) { __builtin_amdgcn_s_sleep(1); \
;     if ((++_sp & 255u) == 0u) { if (xb_ld(&(bar)[XB_TMO])) break; if (_sp > XB_SPIN_CAP) { atomicAdd(&(bar)[XB_TMO], 1u); break; } } } } while (0)
; __device__ __forceinline__ void xcd_barrier(const XcdBarrier& b) {
;     ...
;             XB_SPIN(xb_ld(&bar[XB_XGEN(b.x)]) == gen, bar);
;             __builtin_amdgcn_fence(__ATOMIC_ACQUIRE, "agent");
;             asm volatile("s_waitcnt vmcnt(0)" ::: "memory");
.LBB0_257:
	s_or_b64 exec, exec, s[12:13]
	s_waitcnt vmcnt(0)
	s_waitcnt vmcnt(0)

; __device__ __forceinline__ unsigned xb_ld(unsigned* p)              { return __hip_atomic_load(p, __ATOMIC_RELAXED, __HIP_MEMORY_SCOPE_AGENT); }
; __device__ __forceinline__ unsigned xb_add(unsigned* p, unsigned v) { return __hip_atomic_fetch_add(p, v, __ATOMIC_RELAXED, __HIP_MEMORY_SCOPE_AGENT); }
; #define XB_SPIN(cond, bar) do { unsigned _sp = 0; while (cond) { __builtin_amdgcn_s_sleep(1); \
;     if ((++_sp & 255u) == 0u) { if (xb_ld(&(bar)[XB_TMO])) break; if (_sp > XB_SPIN_CAP) { atomicAdd(&(bar)[XB_TMO], 1u); break; } } } } while (0)
; __device__ __forceinline__ void xcd_barrier(const XcdBarrier& b) {
;     ...
;             const unsigned og = xb_add(&bar[XB_TOP], 1u);
;             const unsigned tg = og / nx;
;             if (og + 1u == (tg + 1u) * nx) xb_add(&bar[XB_TOPGEN], 1u);
;             else XB_SPIN(xb_ld(&bar[XB_TOPGEN]) == tg, bar);
;             __builtin_amdgcn_fence(__ATOMIC_ACQUIRE, "agent");
.LBB0_261:
	s_or_b64 exec, exec, s[12:13]
	v_cvt_f32_u32_e32 v3, v0
	s_waitcnt vmcnt(0)
	v_readfirstlane_b32 s10, v2
	buffer_inv sc1
	s_add_u32 s12, s0, 0x7500
	s_addc_u32 s13, s1, 0
	v_rcp_iflag_f32_e32 v3, v3
	v_add_u32_e32 v1, s10, v1
	v_add_u32_e32 v4, 1, v1
	s_mov_b64 s[14:15], -1
	v_mul_f32_e32 v2, 0x4f7ffffe, v3
	v_cvt_u32_f32_e32 v2, v2
	v_sub_u32_e32 v3, 0, v0
	v_mul_lo_u32 v3, v3, v2
	v_mul_hi_u32 v3, v2, v3
	v_add_u32_e32 v2, v2, v3
	v_mul_hi_u32 v2, v1, v2
	v_mul_lo_u32 v3, v2, v0
	v_sub_u32_e32 v1, v1, v3
	v_add_u32_e32 v5, 1, v2
	v_cmp_ge_u32_e32 vcc, v1, v0
	v_sub_u32_e32 v3, v1, v0
	s_nop 0
	v_cndmask_b32_e32 v2, v2, v5, vcc
	v_cndmask_b32_e32 v1, v1, v3, vcc
	v_add_u32_e32 v3, 1, v2
	v_cmp_ge_u32_e32 vcc, v1, v0
	s_nop 1
	v_cndmask_b32_e32 v2, v2, v3, vcc
	v_mul_lo_u32 v1, v0, v2
	v_add_u32_e32 v0, v1, v0
	v_cmp_ne_u32_e32 vcc, v4, v0
	v_mov_b64_e32 v[0:1], s[12:13]
	s_and_saveexec_b64 s[10:11], vcc
	s_cbranch_execz .LBB0_273
	v_mov_b32_e32 v0, 0
	global_load_dword v1, v0, s[12:13] sc1
	s_mov_b64 s[18:19], 0
	s_waitcnt vmcnt(0)
	v_cmp_eq_u32_e32 vcc, v1, v2
	s_and_saveexec_b64 s[16:17], vcc
	s_cbranch_execz .LBB0_272
	s_add_u32 s14, s0, 0x4200
	s_addc_u32 s15, s1, 0
	s_mov_b32 s28, 1
	s_branch .LBB0_265

; __device__ __forceinline__ unsigned xb_add(unsigned* p, unsigned v) { return __hip_atomic_fetch_add(p, v, __ATOMIC_RELAXED, __HIP_MEMORY_SCOPE_AGENT); }
; __device__ __forceinline__ void xcd_barrier(const XcdBarrier& b) {
;     ...
;             __builtin_amdgcn_fence(__ATOMIC_ACQUIRE, "agent");
;             xb_add(&bar[XB_XGEN(b.x)], 1u);
;             asm volatile("s_waitcnt vmcnt(0)" ::: "memory");
.LBB0_275:
	s_or_b64 exec, exec, s[10:11]
	s_mov_b64 s[10:11], exec
	v_mbcnt_lo_u32_b32 v0, s10, 0
	v_mbcnt_hi_u32_b32 v0, s11, v0
	v_cmp_eq_u32_e32 vcc, 0, v0
	s_waitcnt vmcnt(0)
	s_and_saveexec_b64 s[12:13], vcc
	s_cbranch_execz .LBB0_277
	s_bcnt1_i32_b64 s10, s[10:11]
	v_mov_b32_e32 v0, 0x2000
	v_mov_b32_e32 v1, s10
	global_atomic_add v0, v1, s[8:9] offset:1024

; __device__ __forceinline__ unsigned xb_ld(unsigned* p)              { return __hip_atomic_load(p, __ATOMIC_RELAXED, __HIP_MEMORY_SCOPE_AGENT); }
; __device__ __forceinline__ unsigned xb_add(unsigned* p, unsigned v) { return __hip_atomic_fetch_add(p, v, __ATOMIC_RELAXED, __HIP_MEMORY_SCOPE_AGENT); }
; #define XB_SPIN(cond, bar) do { unsigned _sp = 0; while (cond) { __builtin_amdgcn_s_sleep(1); \
;     if ((++_sp & 255u) == 0u) { if (xb_ld(&(bar)[XB_TMO])) break; if (_sp > XB_SPIN_CAP) { atomicAdd(&(bar)[XB_TMO], 1u); break; } } } } while (0)
; __device__ __forceinline__ void xcd_barrier(const XcdBarrier& b) {
;     ...
;         const unsigned old = xb_add(&bar[XB_XSUB(b.x)], 1u);
;         const unsigned gen = old / nloc;
;         if (old + 1u == (gen + 1u) * nloc) {
;             __builtin_amdgcn_fence(__ATOMIC_RELEASE, "agent");
;             asm volatile("s_waitcnt vmcnt(0)" ::: "memory");
;             const unsigned og = xb_add(&bar[XB_TOP], 1u);
;             const unsigned tg = og / nx;
;             if (og + 1u == (tg + 1u) * nx) xb_add(&bar[XB_TOPGEN], 1u);
;             else XB_SPIN(xb_ld(&bar[XB_TOPGEN]) == tg, bar);
;             __builtin_amdgcn_fence(__ATOMIC_ACQUIRE, "agent");
;             xb_add(&bar[XB_XGEN(b.x)], 1u);
;             asm volatile("s_waitcnt vmcnt(0)" ::: "memory");
;         } else {
;             XB_SPIN(xb_ld(&bar[XB_XGEN(b.x)]) == gen, bar);
;             __builtin_amdgcn_fence(__ATOMIC_ACQUIRE, "agent");
.LBB0_470:
	s_or_b64 exec, exec, s[36:37]
	v_cvt_f32_u32_e32 v5, v3
	s_waitcnt vmcnt(0)
	v_readfirstlane_b32 s7, v4
	v_sub_u32_e32 v4, 0, v3
	v_rcp_iflag_f32_e32 v5, v5
	v_add_u32_e32 v6, s7, v0
	v_mul_f32_e32 v5, 0x4f7ffffe, v5
	v_cvt_u32_f32_e32 v5, v5
	v_mul_lo_u32 v0, v4, v5
	v_mul_hi_u32 v0, v5, v0
	v_add_u32_e32 v0, v5, v0
	v_mul_hi_u32 v0, v6, v0
	v_mul_lo_u32 v4, v0, v3
	v_sub_u32_e32 v4, v6, v4
	v_add_u32_e32 v5, 1, v0
	v_cmp_ge_u32_e32 vcc, v4, v3
	s_nop 1
	v_cndmask_b32_e32 v0, v0, v5, vcc
	v_sub_u32_e32 v5, v4, v3
	v_cndmask_b32_e32 v4, v4, v5, vcc
	v_add_u32_e32 v5, 1, v0
	v_cmp_ge_u32_e32 vcc, v4, v3
	v_add_u32_e32 v4, 1, v6
	s_nop 0
	v_cndmask_b32_e32 v0, v0, v5, vcc
	v_mul_lo_u32 v5, v3, v0
	v_add_u32_e32 v3, v5, v3
	v_cmp_ne_u32_e32 vcc, v4, v3
	s_and_saveexec_b64 s[8:9], vcc
	s_xor_b64 s[36:37], exec, s[8:9]
	s_cbranch_execz .LBB0_484
	buffer_inv sc1
	v_readlane_b32 s8, v252, 4
	v_readlane_b32 s9, v252, 5
	s_waitcnt lgkmcnt(0)
	s_nop 3
	global_load_dword v2, v1, s[8:9] sc1
	s_waitcnt vmcnt(0)
	v_cmp_eq_u32_e32 vcc, v2, v0
	s_and_saveexec_b64 s[38:39], vcc
	s_cbranch_execz .LBB0_483
	s_mov_b32 s7, 1
	s_mov_b64 s[40:41], 0
	s_branch .LBB0_474

; __device__ __forceinline__ unsigned xb_ld(unsigned* p)              { return __hip_atomic_load(p, __ATOMIC_RELAXED, __HIP_MEMORY_SCOPE_AGENT); }
; #define XB_SPIN(cond, bar) do { unsigned _sp = 0; while (cond) { __builtin_amdgcn_s_sleep(1); \
;     if ((++_sp & 255u) == 0u) { if (xb_ld(&(bar)[XB_TMO])) break; if (_sp > XB_SPIN_CAP) { atomicAdd(&(bar)[XB_TMO], 1u); break; } } } } while (0)
; __device__ __forceinline__ void xcd_barrier(const XcdBarrier& b) {
;     ...
;             XB_SPIN(xb_ld(&bar[XB_XGEN(b.x)]) == gen, bar);
;             __builtin_amdgcn_fence(__ATOMIC_ACQUIRE, "agent");
;             asm volatile("s_waitcnt vmcnt(0)" ::: "memory");
.LBB0_483:
	s_or_b64 exec, exec, s[38:39]
	s_waitcnt vmcnt(0)
	s_waitcnt vmcnt(0)

; __device__ __forceinline__ unsigned xb_ld(unsigned* p)              { return __hip_atomic_load(p, __ATOMIC_RELAXED, __HIP_MEMORY_SCOPE_AGENT); }
; __device__ __forceinline__ unsigned xb_add(unsigned* p, unsigned v) { return __hip_atomic_fetch_add(p, v, __ATOMIC_RELAXED, __HIP_MEMORY_SCOPE_AGENT); }
; #define XB_SPIN(cond, bar) do { unsigned _sp = 0; while (cond) { __builtin_amdgcn_s_sleep(1); \
;     if ((++_sp & 255u) == 0u) { if (xb_ld(&(bar)[XB_TMO])) break; if (_sp > XB_SPIN_CAP) { atomicAdd(&(bar)[XB_TMO], 1u); break; } } } } while (0)
; __device__ __forceinline__ void xcd_barrier(const XcdBarrier& b) {
;     ...
;             const unsigned og = xb_add(&bar[XB_TOP], 1u);
;             const unsigned tg = og / nx;
;             if (og + 1u == (tg + 1u) * nx) xb_add(&bar[XB_TOPGEN], 1u);
;             else XB_SPIN(xb_ld(&bar[XB_TOPGEN]) == tg, bar);
;             __builtin_amdgcn_fence(__ATOMIC_ACQUIRE, "agent");
.LBB0_487:
	s_or_b64 exec, exec, s[38:39]
	s_waitcnt vmcnt(0)
	v_readfirstlane_b32 s7, v3
	buffer_inv sc1
	v_sub_u32_e32 v4, 0, v2
	v_readlane_b32 s8, v252, 8
	v_add_u32_e32 v3, s7, v0
	v_cvt_f32_u32_e32 v0, v2
	v_readlane_b32 s9, v252, 9
	s_mov_b64 s[38:39], -1
	v_rcp_iflag_f32_e32 v0, v0
	s_nop 0
	v_mul_f32_e32 v0, 0x4f7ffffe, v0
	v_cvt_u32_f32_e32 v0, v0
	v_mul_lo_u32 v4, v4, v0
	v_mul_hi_u32 v4, v0, v4
	v_add_u32_e32 v0, v0, v4
	v_mul_hi_u32 v0, v3, v0
	v_mul_lo_u32 v4, v0, v2
	v_sub_u32_e32 v4, v3, v4
	v_cmp_ge_u32_e32 vcc, v4, v2
	v_add_u32_e32 v5, 1, v0
	v_add_u32_e32 v3, 1, v3
	v_cndmask_b32_e32 v0, v0, v5, vcc
	v_sub_u32_e32 v5, v4, v2
	v_cndmask_b32_e32 v4, v4, v5, vcc
	v_cmp_ge_u32_e32 vcc, v4, v2
	v_add_u32_e32 v4, 1, v0
	s_nop 0
	v_cndmask_b32_e32 v0, v0, v4, vcc
	v_mul_lo_u32 v4, v2, v0
	v_add_u32_e32 v2, v4, v2
	v_cmp_ne_u32_e32 vcc, v3, v2
	v_mov_b64_e32 v[2:3], s[8:9]
	s_and_saveexec_b64 s[36:37], vcc
	s_cbranch_execz .LBB0_499
	v_readlane_b32 s8, v252, 8
	v_readlane_b32 s9, v252, 9
	s_mov_b64 s[40:41], 0
	s_nop 3
	global_load_dword v2, v1, s[8:9] sc1
	s_waitcnt vmcnt(0)
	v_cmp_eq_u32_e32 vcc, v2, v0
	s_and_saveexec_b64 s[38:39], vcc
	s_cbranch_execz .LBB0_498
	s_mov_b32 s7, 1
	s_branch .LBB0_491

; __device__ __forceinline__ unsigned xb_add(unsigned* p, unsigned v) { return __hip_atomic_fetch_add(p, v, __ATOMIC_RELAXED, __HIP_MEMORY_SCOPE_AGENT); }
; __device__ __forceinline__ void xcd_barrier(const XcdBarrier& b) {
;     ...
;             __builtin_amdgcn_fence(__ATOMIC_ACQUIRE, "agent");
;             xb_add(&bar[XB_XGEN(b.x)], 1u);
;             asm volatile("s_waitcnt vmcnt(0)" ::: "memory");
.LBB0_501:
	s_or_b64 exec, exec, s[36:37]
	s_mov_b64 s[36:37], exec
	v_mbcnt_lo_u32_b32 v0, s36, 0
	v_mbcnt_hi_u32_b32 v0, s37, v0
	v_cmp_eq_u32_e32 vcc, 0, v0
	s_waitcnt vmcnt(0)
	s_and_saveexec_b64 s[38:39], vcc
	s_cbranch_execz .LBB0_503
	s_bcnt1_i32_b64 s7, s[36:37]
	v_readlane_b32 s8, v252, 4
	v_mov_b32_e32 v0, s7
	v_readlane_b32 s9, v252, 5
	s_nop 4
	global_atomic_add v1, v0, s[8:9]

; __device__ __forceinline__ unsigned xb_ld(unsigned* p)              { return __hip_atomic_load(p, __ATOMIC_RELAXED, __HIP_MEMORY_SCOPE_AGENT); }
; __device__ __forceinline__ unsigned xb_add(unsigned* p, unsigned v) { return __hip_atomic_fetch_add(p, v, __ATOMIC_RELAXED, __HIP_MEMORY_SCOPE_AGENT); }
; #define XB_SPIN(cond, bar) do { unsigned _sp = 0; while (cond) { __builtin_amdgcn_s_sleep(1); \
;     if ((++_sp & 255u) == 0u) { if (xb_ld(&(bar)[XB_TMO])) break; if (_sp > XB_SPIN_CAP) { atomicAdd(&(bar)[XB_TMO], 1u); break; } } } } while (0)
; __device__ __forceinline__ void xcd_barrier(const XcdBarrier& b) {
;     ...
;         const unsigned old = xb_add(&bar[XB_XSUB(b.x)], 1u);
;         const unsigned gen = old / nloc;
;         if (old + 1u == (gen + 1u) * nloc) {
;             __builtin_amdgcn_fence(__ATOMIC_RELEASE, "agent");
;             asm volatile("s_waitcnt vmcnt(0)" ::: "memory");
;             const unsigned og = xb_add(&bar[XB_TOP], 1u);
;             const unsigned tg = og / nx;
;             if (og + 1u == (tg + 1u) * nx) xb_add(&bar[XB_TOPGEN], 1u);
;             else XB_SPIN(xb_ld(&bar[XB_TOPGEN]) == tg, bar);
;             __builtin_amdgcn_fence(__ATOMIC_ACQUIRE, "agent");
;             xb_add(&bar[XB_XGEN(b.x)], 1u);
;             asm volatile("s_waitcnt vmcnt(0)" ::: "memory");
;         } else {
;             XB_SPIN(xb_ld(&bar[XB_XGEN(b.x)]) == gen, bar);
;             __builtin_amdgcn_fence(__ATOMIC_ACQUIRE, "agent");
.LBB0_736:
	s_or_b64 exec, exec, s[36:37]
	v_cvt_f32_u32_e32 v5, v3
	s_waitcnt vmcnt(0)
	v_readfirstlane_b32 s6, v4
	v_sub_u32_e32 v4, 0, v3
	v_rcp_iflag_f32_e32 v5, v5
	v_add_u32_e32 v6, s6, v0
	v_mul_f32_e32 v5, 0x4f7ffffe, v5
	v_cvt_u32_f32_e32 v5, v5
	v_mul_lo_u32 v0, v4, v5
	v_mul_hi_u32 v0, v5, v0
	v_add_u32_e32 v0, v5, v0
	v_mul_hi_u32 v0, v6, v0
	v_mul_lo_u32 v4, v0, v3
	v_sub_u32_e32 v4, v6, v4
	v_add_u32_e32 v5, 1, v0
	v_cmp_ge_u32_e32 vcc, v4, v3
	s_nop 1
	v_cndmask_b32_e32 v0, v0, v5, vcc
	v_sub_u32_e32 v5, v4, v3
	v_cndmask_b32_e32 v4, v4, v5, vcc
	v_add_u32_e32 v5, 1, v0
	v_cmp_ge_u32_e32 vcc, v4, v3
	v_add_u32_e32 v4, 1, v6
	s_nop 0
	v_cndmask_b32_e32 v0, v0, v5, vcc
	v_mul_lo_u32 v5, v3, v0
	v_add_u32_e32 v3, v5, v3
	v_cmp_ne_u32_e32 vcc, v4, v3
	s_and_saveexec_b64 s[6:7], vcc
	s_xor_b64 s[36:37], exec, s[6:7]
	s_cbranch_execz .LBB0_750
	buffer_inv sc1
	v_readlane_b32 s6, v252, 4
	v_readlane_b32 s7, v252, 5
	s_waitcnt lgkmcnt(0)
	s_nop 3
	global_load_dword v2, v1, s[6:7] sc1
	s_waitcnt vmcnt(0)
	v_cmp_eq_u32_e32 vcc, v2, v0
	s_and_saveexec_b64 s[38:39], vcc
	s_cbranch_execz .LBB0_749
	s_mov_b32 s6, 1
	s_mov_b64 s[40:41], 0
	s_branch .LBB0_740

; __device__ __forceinline__ unsigned xb_ld(unsigned* p)              { return __hip_atomic_load(p, __ATOMIC_RELAXED, __HIP_MEMORY_SCOPE_AGENT); }
; __device__ __forceinline__ unsigned xb_add(unsigned* p, unsigned v) { return __hip_atomic_fetch_add(p, v, __ATOMIC_RELAXED, __HIP_MEMORY_SCOPE_AGENT); }
; #define XB_SPIN(cond, bar) do { unsigned _sp = 0; while (cond) { __builtin_amdgcn_s_sleep(1); \
;     if ((++_sp & 255u) == 0u) { if (xb_ld(&(bar)[XB_TMO])) break; if (_sp > XB_SPIN_CAP) { atomicAdd(&(bar)[XB_TMO], 1u); break; } } } } while (0)
; __device__ __forceinline__ void xcd_barrier(const XcdBarrier& b) {
;     ...
;             const unsigned og = xb_add(&bar[XB_TOP], 1u);
;             const unsigned tg = og / nx;
;             if (og + 1u == (tg + 1u) * nx) xb_add(&bar[XB_TOPGEN], 1u);
;             else XB_SPIN(xb_ld(&bar[XB_TOPGEN]) == tg, bar);
;             __builtin_amdgcn_fence(__ATOMIC_ACQUIRE, "agent");
.LBB0_753:
	s_or_b64 exec, exec, s[38:39]
	s_waitcnt vmcnt(0)
	v_readfirstlane_b32 s6, v3
	buffer_inv sc1
	v_sub_u32_e32 v4, 0, v2
	s_mov_b64 s[38:39], -1
	v_add_u32_e32 v3, s6, v0
	v_cvt_f32_u32_e32 v0, v2
	v_readlane_b32 s6, v252, 8
	v_readlane_b32 s7, v252, 9
	v_rcp_iflag_f32_e32 v0, v0
	s_nop 0
	v_mul_f32_e32 v0, 0x4f7ffffe, v0
	v_cvt_u32_f32_e32 v0, v0
	v_mul_lo_u32 v4, v4, v0
	v_mul_hi_u32 v4, v0, v4
	v_add_u32_e32 v0, v0, v4
	v_mul_hi_u32 v0, v3, v0
	v_mul_lo_u32 v4, v0, v2
	v_sub_u32_e32 v4, v3, v4
	v_cmp_ge_u32_e32 vcc, v4, v2
	v_add_u32_e32 v5, 1, v0
	v_add_u32_e32 v3, 1, v3
	v_cndmask_b32_e32 v0, v0, v5, vcc
	v_sub_u32_e32 v5, v4, v2
	v_cndmask_b32_e32 v4, v4, v5, vcc
	v_cmp_ge_u32_e32 vcc, v4, v2
	v_add_u32_e32 v4, 1, v0
	s_nop 0
	v_cndmask_b32_e32 v0, v0, v4, vcc
	v_mul_lo_u32 v4, v2, v0
	v_add_u32_e32 v2, v4, v2
	v_cmp_ne_u32_e32 vcc, v3, v2
	v_mov_b64_e32 v[2:3], s[6:7]
	s_and_saveexec_b64 s[36:37], vcc
	s_cbranch_execz .LBB0_765
	v_readlane_b32 s6, v252, 8
	v_readlane_b32 s7, v252, 9
	s_mov_b64 s[40:41], 0
	s_nop 3
	global_load_dword v2, v1, s[6:7] sc1
	s_waitcnt vmcnt(0)
	v_cmp_eq_u32_e32 vcc, v2, v0
	s_and_saveexec_b64 s[38:39], vcc
	s_cbranch_execz .LBB0_764
	s_mov_b32 s6, 1
	s_branch .LBB0_757

; __device__ __forceinline__ unsigned xb_add(unsigned* p, unsigned v) { return __hip_atomic_fetch_add(p, v, __ATOMIC_RELAXED, __HIP_MEMORY_SCOPE_AGENT); }
; __device__ __forceinline__ void xcd_barrier(const XcdBarrier& b) {
;     ...
;             __builtin_amdgcn_fence(__ATOMIC_ACQUIRE, "agent");
;             xb_add(&bar[XB_XGEN(b.x)], 1u);
;             asm volatile("s_waitcnt vmcnt(0)" ::: "memory");
.LBB0_767:
	s_or_b64 exec, exec, s[36:37]
	s_mov_b64 s[36:37], exec
	v_mbcnt_lo_u32_b32 v0, s36, 0
	v_mbcnt_hi_u32_b32 v0, s37, v0
	v_cmp_eq_u32_e32 vcc, 0, v0
	s_waitcnt vmcnt(0)
	s_and_saveexec_b64 s[38:39], vcc
	s_cbranch_execz .LBB0_769
	s_bcnt1_i32_b64 s6, s[36:37]
	v_mov_b32_e32 v0, s6
	v_readlane_b32 s6, v252, 4
	v_readlane_b32 s7, v252, 5
	s_nop 4
	global_atomic_add v1, v0, s[6:7]

; __device__ __forceinline__ unsigned xb_ld(unsigned* p)              { return __hip_atomic_load(p, __ATOMIC_RELAXED, __HIP_MEMORY_SCOPE_AGENT); }
; __device__ __forceinline__ unsigned xb_add(unsigned* p, unsigned v) { return __hip_atomic_fetch_add(p, v, __ATOMIC_RELAXED, __HIP_MEMORY_SCOPE_AGENT); }
; #define XB_SPIN(cond, bar) do { unsigned _sp = 0; while (cond) { __builtin_amdgcn_s_sleep(1); \
;     if ((++_sp & 255u) == 0u) { if (xb_ld(&(bar)[XB_TMO])) break; if (_sp > XB_SPIN_CAP) { atomicAdd(&(bar)[XB_TMO], 1u); break; } } } } while (0)
; __device__ __forceinline__ void xcd_barrier(const XcdBarrier& b) {
;     ...
;         const unsigned old = xb_add(&bar[XB_XSUB(b.x)], 1u);
;         const unsigned gen = old / nloc;
;         if (old + 1u == (gen + 1u) * nloc) {
;             __builtin_amdgcn_fence(__ATOMIC_RELEASE, "agent");
;             asm volatile("s_waitcnt vmcnt(0)" ::: "memory");
;             const unsigned og = xb_add(&bar[XB_TOP], 1u);
;             const unsigned tg = og / nx;
;             if (og + 1u == (tg + 1u) * nx) xb_add(&bar[XB_TOPGEN], 1u);
;             else XB_SPIN(xb_ld(&bar[XB_TOPGEN]) == tg, bar);
;             __builtin_amdgcn_fence(__ATOMIC_ACQUIRE, "agent");
;             xb_add(&bar[XB_XGEN(b.x)], 1u);
;             asm volatile("s_waitcnt vmcnt(0)" ::: "memory");
;         } else {
;             XB_SPIN(xb_ld(&bar[XB_XGEN(b.x)]) == gen, bar);
;             __builtin_amdgcn_fence(__ATOMIC_ACQUIRE, "agent");
.LBB0_1341:
	s_or_b64 exec, exec, s[38:39]
	v_cvt_f32_u32_e32 v5, v3
	s_waitcnt vmcnt(0)
	v_readfirstlane_b32 s7, v4
	v_sub_u32_e32 v4, 0, v3
	v_rcp_iflag_f32_e32 v5, v5
	v_add_u32_e32 v6, s7, v0
	v_mul_f32_e32 v5, 0x4f7ffffe, v5
	v_cvt_u32_f32_e32 v5, v5
	v_mul_lo_u32 v0, v4, v5
	v_mul_hi_u32 v0, v5, v0
	v_add_u32_e32 v0, v5, v0
	v_mul_hi_u32 v0, v6, v0
	v_mul_lo_u32 v4, v0, v3
	v_sub_u32_e32 v4, v6, v4
	v_add_u32_e32 v5, 1, v0
	v_cmp_ge_u32_e32 vcc, v4, v3
	s_nop 1
	v_cndmask_b32_e32 v0, v0, v5, vcc
	v_sub_u32_e32 v5, v4, v3
	v_cndmask_b32_e32 v4, v4, v5, vcc
	v_add_u32_e32 v5, 1, v0
	v_cmp_ge_u32_e32 vcc, v4, v3
	v_add_u32_e32 v4, 1, v6
	s_nop 0
	v_cndmask_b32_e32 v0, v0, v5, vcc
	v_mul_lo_u32 v5, v3, v0
	v_add_u32_e32 v3, v5, v3
	v_cmp_ne_u32_e32 vcc, v4, v3
	s_and_saveexec_b64 s[8:9], vcc
	s_xor_b64 s[38:39], exec, s[8:9]
	s_cbranch_execz .LBB0_1355
	buffer_inv sc1
	v_readlane_b32 s8, v252, 4
	v_readlane_b32 s9, v252, 5
	s_waitcnt lgkmcnt(0)
	s_nop 3
	global_load_dword v2, v1, s[8:9] sc1
	s_waitcnt vmcnt(0)
	v_cmp_eq_u32_e32 vcc, v2, v0
	s_and_saveexec_b64 s[40:41], vcc
	s_cbranch_execz .LBB0_1354
	s_mov_b32 s7, 1
	s_mov_b64 s[44:45], 0
	s_branch .LBB0_1345

; __device__ __forceinline__ unsigned xb_ld(unsigned* p)              { return __hip_atomic_load(p, __ATOMIC_RELAXED, __HIP_MEMORY_SCOPE_AGENT); }
; #define XB_SPIN(cond, bar) do { unsigned _sp = 0; while (cond) { __builtin_amdgcn_s_sleep(1); \
;     if ((++_sp & 255u) == 0u) { if (xb_ld(&(bar)[XB_TMO])) break; if (_sp > XB_SPIN_CAP) { atomicAdd(&(bar)[XB_TMO], 1u); break; } } } } while (0)
; __device__ __forceinline__ void xcd_barrier(const XcdBarrier& b) {
;     ...
;             XB_SPIN(xb_ld(&bar[XB_XGEN(b.x)]) == gen, bar);
;             __builtin_amdgcn_fence(__ATOMIC_ACQUIRE, "agent");
;             asm volatile("s_waitcnt vmcnt(0)" ::: "memory");
.LBB0_1354:
	s_or_b64 exec, exec, s[40:41]
	s_waitcnt vmcnt(0)
	s_waitcnt vmcnt(0)

; __device__ __forceinline__ unsigned xb_ld(unsigned* p)              { return __hip_atomic_load(p, __ATOMIC_RELAXED, __HIP_MEMORY_SCOPE_AGENT); }
; __device__ __forceinline__ unsigned xb_add(unsigned* p, unsigned v) { return __hip_atomic_fetch_add(p, v, __ATOMIC_RELAXED, __HIP_MEMORY_SCOPE_AGENT); }
; #define XB_SPIN(cond, bar) do { unsigned _sp = 0; while (cond) { __builtin_amdgcn_s_sleep(1); \
;     if ((++_sp & 255u) == 0u) { if (xb_ld(&(bar)[XB_TMO])) break; if (_sp > XB_SPIN_CAP) { atomicAdd(&(bar)[XB_TMO], 1u); break; } } } } while (0)
; __device__ __forceinline__ void xcd_barrier(const XcdBarrier& b) {
;     ...
;             const unsigned og = xb_add(&bar[XB_TOP], 1u);
;             const unsigned tg = og / nx;
;             if (og + 1u == (tg + 1u) * nx) xb_add(&bar[XB_TOPGEN], 1u);
;             else XB_SPIN(xb_ld(&bar[XB_TOPGEN]) == tg, bar);
;             __builtin_amdgcn_fence(__ATOMIC_ACQUIRE, "agent");
.LBB0_1358:
	s_or_b64 exec, exec, s[40:41]
	s_waitcnt vmcnt(0)
	v_readfirstlane_b32 s7, v3
	buffer_inv sc1
	v_sub_u32_e32 v4, 0, v2
	v_readlane_b32 s8, v252, 8
	v_add_u32_e32 v3, s7, v0
	v_cvt_f32_u32_e32 v0, v2
	v_readlane_b32 s9, v252, 9
	s_mov_b64 s[40:41], -1
	v_rcp_iflag_f32_e32 v0, v0
	s_nop 0
	v_mul_f32_e32 v0, 0x4f7ffffe, v0
	v_cvt_u32_f32_e32 v0, v0
	v_mul_lo_u32 v4, v4, v0
	v_mul_hi_u32 v4, v0, v4
	v_add_u32_e32 v0, v0, v4
	v_mul_hi_u32 v0, v3, v0
	v_mul_lo_u32 v4, v0, v2
	v_sub_u32_e32 v4, v3, v4
	v_cmp_ge_u32_e32 vcc, v4, v2
	v_add_u32_e32 v5, 1, v0
	v_add_u32_e32 v3, 1, v3
	v_cndmask_b32_e32 v0, v0, v5, vcc
	v_sub_u32_e32 v5, v4, v2
	v_cndmask_b32_e32 v4, v4, v5, vcc
	v_cmp_ge_u32_e32 vcc, v4, v2
	v_add_u32_e32 v4, 1, v0
	s_nop 0
	v_cndmask_b32_e32 v0, v0, v4, vcc
	v_mul_lo_u32 v4, v2, v0
	v_add_u32_e32 v2, v4, v2
	v_cmp_ne_u32_e32 vcc, v3, v2
	v_mov_b64_e32 v[2:3], s[8:9]
	s_and_saveexec_b64 s[38:39], vcc
	s_cbranch_execz .LBB0_1370
	v_readlane_b32 s8, v252, 8
	v_readlane_b32 s9, v252, 9
	s_mov_b64 s[44:45], 0
	s_nop 3
	global_load_dword v2, v1, s[8:9] sc1
	s_waitcnt vmcnt(0)
	v_cmp_eq_u32_e32 vcc, v2, v0
	s_and_saveexec_b64 s[40:41], vcc
	s_cbranch_execz .LBB0_1369
	s_mov_b32 s7, 1
	s_branch .LBB0_1362

; __device__ __forceinline__ unsigned xb_add(unsigned* p, unsigned v) { return __hip_atomic_fetch_add(p, v, __ATOMIC_RELAXED, __HIP_MEMORY_SCOPE_AGENT); }
; __device__ __forceinline__ void xcd_barrier(const XcdBarrier& b) {
;     ...
;             __builtin_amdgcn_fence(__ATOMIC_ACQUIRE, "agent");
;             xb_add(&bar[XB_XGEN(b.x)], 1u);
;             asm volatile("s_waitcnt vmcnt(0)" ::: "memory");
.LBB0_1372:
	s_or_b64 exec, exec, s[38:39]
	s_mov_b64 s[38:39], exec
	v_mbcnt_lo_u32_b32 v0, s38, 0
	v_mbcnt_hi_u32_b32 v0, s39, v0
	v_cmp_eq_u32_e32 vcc, 0, v0
	s_waitcnt vmcnt(0)
	s_and_saveexec_b64 s[40:41], vcc
	s_cbranch_execz .LBB0_1374
	s_bcnt1_i32_b64 s7, s[38:39]
	v_readlane_b32 s8, v252, 4
	v_mov_b32_e32 v0, s7
	v_readlane_b32 s9, v252, 5
	s_nop 4
	global_atomic_add v1, v0, s[8:9]

; __device__ __forceinline__ unsigned xb_add(unsigned* p, unsigned v) { return __hip_atomic_fetch_add(p, v, __ATOMIC_RELAXED, __HIP_MEMORY_SCOPE_AGENT); }
; __device__ __forceinline__ void xcd_barrier(const XcdBarrier& b) {
;     ...
;             __builtin_amdgcn_fence(__ATOMIC_ACQUIRE, "agent");
;             xb_add(&bar[XB_XGEN(b.x)], 1u);
;             asm volatile("s_waitcnt vmcnt(0)" ::: "memory");
.LBB0_1692:
	s_or_b64 exec, exec, s[36:37]
	s_mov_b64 s[36:37], exec
	v_mbcnt_lo_u32_b32 v0, s36, 0
	v_mbcnt_hi_u32_b32 v0, s37, v0
	v_cmp_eq_u32_e32 vcc, 0, v0
	s_waitcnt vmcnt(0)
	s_and_saveexec_b64 s[38:39], vcc
	s_cbranch_execz .LBB0_1549
	s_bcnt1_i32_b64 s6, s[36:37]
	v_mov_b32_e32 v0, s6
	v_readlane_b32 s6, v252, 4
	v_readlane_b32 s7, v252, 5
	s_nop 4
	global_atomic_add v1, v0, s[6:7]
	s_branch .LBB0_1549
